# baseline (speedup 1.0000x reference)
.Lc2_bar_6:
	s_barrier
	s_waitcnt lgkmcnt(5)
	v_mfma_f32_16x16x32_f16 v[110:113], v[26:29], v[34:37], v[110:113]
	ds_read_b128 v[142:145], v174
	s_mul_i32 s79, s29, 0
	s_add_i32 s79, s79, 17
	s_add_i32 s79, s79, s78
	s_lshl_b32 s68, s79, 15
	s_waitcnt lgkmcnt(5)
	v_mfma_f32_16x16x32_f16 v[106:109], v[22:25], v[34:37], v[106:109]
	v_add_u32_e32 v182, 69, v130
	v_bitop3_b32 v183, v182, v129, 6 bitop3:0x6c
	v_lshl_add_u32 v182, v182, 7, s80
	v_mfma_f32_16x16x32_f16 v[94:97], v[26:29], v[30:33], v[94:97]
	ds_read_b128 v[146:149], v174 offset:2048
	v_lshl_add_u64 v[178:179], v[126:127], 0, s[68:69]
	s_and_b32 s70, s34, 0xc000
	s_add_i32 s70, s70, s33
	v_mfma_f32_16x16x32_f16 v[90:93], v[22:25], v[30:33], v[90:93]
	v_lshl_or_b32 v176, v183, 4, v182
	v_xor_b32_e32 v176, s81, v176
	s_waitcnt lgkmcnt(5)
	v_mfma_f32_16x16x32_f16 v[74:77], v[26:29], v[42:45], v[74:77]
	ds_read_b128 v[150:153], v176
	v_mfma_f32_16x16x32_f16 v[58:61], v[22:25], v[42:45], v[58:61]
	v_add_u32_e32 v182, 103, v130
	v_bitop3_b32 v183, v182, v129, 6 bitop3:0x6c
	v_lshl_add_u32 v182, v182, 7, s80
	s_waitcnt lgkmcnt(5)
	v_mfma_f32_16x16x32_f16 v[78:81], v[26:29], v[38:41], v[78:81]
	ds_read_b128 v[154:157], v176 offset:2048
	v_mfma_f32_16x16x32_f16 v[62:65], v[22:25], v[38:41], v[62:65]
	v_lshl_or_b32 v177, v183, 4, v182
	v_xor_b32_e32 v177, s81, v177
	s_mov_b32 m0, s70
	s_add_i32 s71, s34, 0xffff8000
	global_load_lds_dwordx4 v[178:179], off
	s_waitcnt lgkmcnt(5)
	v_mfma_f32_16x16x32_f16 v[102:105], v[54:57], v[34:37], v[102:105]
	ds_read_b128 v[158:161], v177
	s_waitcnt lgkmcnt(5)
	v_mfma_f32_16x16x32_f16 v[98:101], v[50:53], v[34:37], v[98:101]
	s_and_b32 s71, s71, 0xc000
	s_add_i32 s72, s70, 0x400
	v_lshl_add_u64 v[180:181], v[178:179], 0, s[16:17]
	v_mfma_f32_16x16x32_f16 v[86:89], v[54:57], v[30:33], v[86:89]
	ds_read_b128 v[162:165], v177 offset:2048
	v_mfma_f32_16x16x32_f16 v[82:85], v[50:53], v[30:33], v[82:85]
	v_add_u32_e32 v175, s71, v184
	v_mfma_f32_16x16x32_f16 v[46:49], v[54:57], v[42:45], v[46:49]
	ds_read_b128 v[166:169], v174 offset:4096
	v_mfma_f32_16x16x32_f16 v[18:21], v[50:53], v[42:45], v[18:21]
	v_mfma_f32_16x16x32_f16 v[70:73], v[54:57], v[38:41], v[70:73]
	ds_read_b128 v[170:173], v174 offset:6144
	v_mfma_f32_16x16x32_f16 v[66:69], v[50:53], v[38:41], v[66:69]
	v_add_u32_e32 v174, s71, v185
	s_waitcnt lgkmcnt(7)
	v_mfma_f32_16x16x32_f16 v[110:113], v[142:145], v[42:45], v[110:113]
	ds_read_b128 v[26:29], v175
	s_waitcnt lgkmcnt(7)
	v_mfma_f32_16x16x32_f16 v[106:109], v[146:149], v[42:45], v[106:109]
	v_add_u32_e32 v182, 2, v130
	v_bitop3_b32 v183, v182, v129, 6 bitop3:0x6c
	v_lshl_add_u32 v182, v182, 7, s80
	v_mfma_f32_16x16x32_f16 v[94:97], v[142:145], v[38:41], v[94:97]
	ds_read_b128 v[22:25], v175 offset:2048
	v_mfma_f32_16x16x32_f16 v[90:93], v[146:149], v[38:41], v[90:93]
	v_lshl_or_b32 v176, v183, 4, v182
	v_xor_b32_e32 v176, s81, v176
	s_waitcnt lgkmcnt(7)
	v_mfma_f32_16x16x32_f16 v[74:77], v[142:145], v[150:153], v[74:77]
	ds_read_b128 v[34:37], v176
	v_mfma_f32_16x16x32_f16 v[58:61], v[146:149], v[150:153], v[58:61]
	s_waitcnt lgkmcnt(7)
	v_mfma_f32_16x16x32_f16 v[78:81], v[142:145], v[154:157], v[78:81]
	ds_read_b128 v[30:33], v176 offset:2048
	v_mfma_f32_16x16x32_f16 v[62:65], v[146:149], v[154:157], v[62:65]
	s_mov_b32 m0, s72
	s_addk_i32 s34, 0x4000
	global_load_lds_dwordx4 v[180:181], off
	s_waitcnt lgkmcnt(5)
	v_mfma_f32_16x16x32_f16 v[102:105], v[166:169], v[42:45], v[102:105]
	s_waitcnt lgkmcnt(4)
	v_mfma_f32_16x16x32_f16 v[98:101], v[170:173], v[42:45], v[98:101]
	v_mfma_f32_16x16x32_f16 v[86:89], v[166:169], v[38:41], v[86:89]
	v_mfma_f32_16x16x32_f16 v[82:85], v[170:173], v[38:41], v[82:85]
	v_mfma_f32_16x16x32_f16 v[46:49], v[166:169], v[150:153], v[46:49]
	ds_read_b128 v[54:57], v175 offset:4096
	v_mfma_f32_16x16x32_f16 v[18:21], v[170:173], v[150:153], v[18:21]
	v_mfma_f32_16x16x32_f16 v[70:73], v[166:169], v[154:157], v[70:73]
	ds_read_b128 v[50:53], v175 offset:6144
	v_mfma_f32_16x16x32_f16 v[66:69], v[170:173], v[154:157], v[66:69]
	s_cmp_eq_u32 s67, 0
	s_cbranch_scc1 .Lc2_w2_7
	s_waitcnt vmcnt(8)
	s_sub_i32 s67, s67, 1
	s_branch .Lc2_bar_7

.Lc2_bar_7:
	s_barrier
	s_waitcnt lgkmcnt(5)
	v_mfma_f32_16x16x32_f16 v[110:113], v[26:29], v[150:153], v[110:113]
	ds_read_b128 v[142:145], v174
	s_mul_i32 s79, s29, 0
	s_add_i32 s79, s79, 17
	s_add_i32 s79, s79, s78
	s_lshl_b32 s68, s79, 15
	s_waitcnt lgkmcnt(5)
	v_mfma_f32_16x16x32_f16 v[106:109], v[22:25], v[150:153], v[106:109]
	v_add_u32_e32 v182, 36, v130
	v_bitop3_b32 v183, v182, v129, 6 bitop3:0x6c
	v_lshl_add_u32 v182, v182, 7, s80
	v_mfma_f32_16x16x32_f16 v[94:97], v[26:29], v[154:157], v[94:97]
	ds_read_b128 v[146:149], v174 offset:2048
	v_lshl_add_u64 v[178:179], v[126:127], 0, s[68:69]
	s_and_b32 s70, s34, 0xc000
	s_add_i32 s70, s70, s33
	v_mfma_f32_16x16x32_f16 v[90:93], v[22:25], v[154:157], v[90:93]
	v_lshl_or_b32 v176, v183, 4, v182
	v_xor_b32_e32 v176, s81, v176
	v_mfma_f32_16x16x32_f16 v[74:77], v[26:29], v[158:161], v[74:77]
	ds_read_b128 v[42:45], v176
	v_mfma_f32_16x16x32_f16 v[58:61], v[22:25], v[158:161], v[58:61]
	v_mfma_f32_16x16x32_f16 v[78:81], v[26:29], v[162:165], v[78:81]
	ds_read_b128 v[38:41], v176 offset:2048
	v_mfma_f32_16x16x32_f16 v[62:65], v[22:25], v[162:165], v[62:65]
	s_mov_b32 m0, s70
	s_add_i32 s71, s34, 0xffff8000
	global_load_lds_dwordx4 v[178:179], off
	s_waitcnt lgkmcnt(5)
	v_mfma_f32_16x16x32_f16 v[102:105], v[54:57], v[150:153], v[102:105]
	s_waitcnt lgkmcnt(4)
	v_mfma_f32_16x16x32_f16 v[98:101], v[50:53], v[150:153], v[98:101]
	s_and_b32 s71, s71, 0xc000
	s_add_i32 s72, s70, 0x400
	v_lshl_add_u64 v[180:181], v[178:179], 0, s[16:17]
	v_mfma_f32_16x16x32_f16 v[86:89], v[54:57], v[154:157], v[86:89]
	v_mfma_f32_16x16x32_f16 v[82:85], v[50:53], v[154:157], v[82:85]
	v_add_u32_e32 v175, s71, v184
	v_mfma_f32_16x16x32_f16 v[46:49], v[54:57], v[158:161], v[46:49]
	ds_read_b128 v[166:169], v174 offset:4096
	v_mfma_f32_16x16x32_f16 v[18:21], v[50:53], v[158:161], v[18:21]
	v_mfma_f32_16x16x32_f16 v[70:73], v[54:57], v[162:165], v[70:73]
	ds_read_b128 v[170:173], v174 offset:6144
	v_mfma_f32_16x16x32_f16 v[66:69], v[50:53], v[162:165], v[66:69]
	v_add_u32_e32 v174, s71, v185
	s_waitcnt lgkmcnt(5)
	v_mfma_f32_16x16x32_f16 v[110:113], v[142:145], v[34:37], v[110:113]
	ds_read_b128 v[26:29], v175
	s_waitcnt lgkmcnt(5)
	v_mfma_f32_16x16x32_f16 v[106:109], v[146:149], v[34:37], v[106:109]
	v_add_u32_e32 v182, 70, v130
	v_bitop3_b32 v183, v182, v129, 6 bitop3:0x6c
	v_lshl_add_u32 v182, v182, 7, s80
	v_mfma_f32_16x16x32_f16 v[94:97], v[142:145], v[30:33], v[94:97]
	ds_read_b128 v[22:25], v175 offset:2048
	v_mfma_f32_16x16x32_f16 v[90:93], v[146:149], v[30:33], v[90:93]
	v_lshl_or_b32 v176, v183, 4, v182
	v_xor_b32_e32 v176, s81, v176
	s_waitcnt lgkmcnt(5)
	v_mfma_f32_16x16x32_f16 v[74:77], v[142:145], v[42:45], v[74:77]
	ds_read_b128 v[150:153], v176
	v_mfma_f32_16x16x32_f16 v[58:61], v[146:149], v[42:45], v[58:61]
	v_add_u32_e32 v182, 104, v130
	v_bitop3_b32 v183, v182, v129, 6 bitop3:0x6c
	v_lshl_add_u32 v182, v182, 7, s80
	s_waitcnt lgkmcnt(5)
	v_mfma_f32_16x16x32_f16 v[78:81], v[142:145], v[38:41], v[78:81]
	ds_read_b128 v[154:157], v176 offset:2048
	v_mfma_f32_16x16x32_f16 v[62:65], v[146:149], v[38:41], v[62:65]
	v_lshl_or_b32 v177, v183, 4, v182
	v_xor_b32_e32 v177, s81, v177
	s_mov_b32 m0, s72
	s_addk_i32 s34, 0x4000
	global_load_lds_dwordx4 v[180:181], off
	s_waitcnt lgkmcnt(5)
	v_mfma_f32_16x16x32_f16 v[102:105], v[166:169], v[34:37], v[102:105]
	ds_read_b128 v[158:161], v177
	s_waitcnt lgkmcnt(5)
	v_mfma_f32_16x16x32_f16 v[98:101], v[170:173], v[34:37], v[98:101]
	v_mfma_f32_16x16x32_f16 v[86:89], v[166:169], v[30:33], v[86:89]
	ds_read_b128 v[162:165], v177 offset:2048
	v_mfma_f32_16x16x32_f16 v[82:85], v[170:173], v[30:33], v[82:85]
	v_mfma_f32_16x16x32_f16 v[46:49], v[166:169], v[42:45], v[46:49]
	ds_read_b128 v[54:57], v175 offset:4096
	v_mfma_f32_16x16x32_f16 v[18:21], v[170:173], v[42:45], v[18:21]
	v_mfma_f32_16x16x32_f16 v[70:73], v[166:169], v[38:41], v[70:73]
	ds_read_b128 v[50:53], v175 offset:6144
	v_mfma_f32_16x16x32_f16 v[66:69], v[170:173], v[38:41], v[66:69]
	s_cmp_eq_u32 s67, 0
	s_cbranch_scc1 .Lc2_w2_8
	s_waitcnt vmcnt(8)
	s_sub_i32 s67, s67, 1
	s_branch .Lc2_bar_8

.Lc2_bar_8:
	s_barrier
	s_waitcnt lgkmcnt(7)
	v_mfma_f32_16x16x32_f16 v[110:113], v[26:29], v[42:45], v[110:113]
	ds_read_b128 v[142:145], v174
	s_mul_i32 s79, s29, 0
	s_add_i32 s79, s79, 17
	s_add_i32 s79, s79, s78
	s_lshl_b32 s68, s79, 15
	s_waitcnt lgkmcnt(7)
	v_mfma_f32_16x16x32_f16 v[106:109], v[22:25], v[42:45], v[106:109]
	v_mov_b32_e32 v182, v130
	v_bitop3_b32 v183, v182, v129, 6 bitop3:0x6c
	v_lshl_add_u32 v182, v182, 7, 0
	v_mfma_f32_16x16x32_f16 v[94:97], v[26:29], v[38:41], v[94:97]
	ds_read_b128 v[146:149], v174 offset:2048
	v_lshl_add_u64 v[178:179], v[126:127], 0, s[68:69]
	s_and_b32 s70, s34, 0xc000
	s_add_i32 s70, s70, s33
	v_mfma_f32_16x16x32_f16 v[90:93], v[22:25], v[38:41], v[90:93]
	v_lshl_or_b32 v176, v183, 4, v182
	v_xor_b32_e32 v176, s81, v176
	s_waitcnt lgkmcnt(7)
	v_mfma_f32_16x16x32_f16 v[74:77], v[26:29], v[150:153], v[74:77]
	ds_read_b128 v[34:37], v176
	v_mfma_f32_16x16x32_f16 v[58:61], v[22:25], v[150:153], v[58:61]
	s_waitcnt lgkmcnt(7)
	v_mfma_f32_16x16x32_f16 v[78:81], v[26:29], v[154:157], v[78:81]
	ds_read_b128 v[30:33], v176 offset:2048
	v_mfma_f32_16x16x32_f16 v[62:65], v[22:25], v[154:157], v[62:65]
	s_mov_b32 m0, s70
	s_add_i32 s71, s34, 0xffff8000
	global_load_lds_dwordx4 v[178:179], off
	s_waitcnt lgkmcnt(5)
	v_mfma_f32_16x16x32_f16 v[102:105], v[54:57], v[42:45], v[102:105]
	s_waitcnt lgkmcnt(4)
	v_mfma_f32_16x16x32_f16 v[98:101], v[50:53], v[42:45], v[98:101]
	s_and_b32 s71, s71, 0xc000
	s_add_i32 s72, s70, 0x400
	v_lshl_add_u64 v[180:181], v[178:179], 0, s[16:17]
	v_mfma_f32_16x16x32_f16 v[86:89], v[54:57], v[38:41], v[86:89]
	v_mfma_f32_16x16x32_f16 v[82:85], v[50:53], v[38:41], v[82:85]
	v_add_u32_e32 v175, s71, v184
	v_mfma_f32_16x16x32_f16 v[46:49], v[54:57], v[150:153], v[46:49]
	ds_read_b128 v[166:169], v174 offset:4096
	v_mfma_f32_16x16x32_f16 v[18:21], v[50:53], v[150:153], v[18:21]
	v_mfma_f32_16x16x32_f16 v[70:73], v[54:57], v[154:157], v[70:73]
	ds_read_b128 v[170:173], v174 offset:6144
	v_mfma_f32_16x16x32_f16 v[66:69], v[50:53], v[154:157], v[66:69]
	v_add_u32_e32 v174, s71, v185
	s_waitcnt lgkmcnt(5)
	v_mfma_f32_16x16x32_f16 v[110:113], v[142:145], v[150:153], v[110:113]
	ds_read_b128 v[26:29], v175
	s_waitcnt lgkmcnt(5)
	v_mfma_f32_16x16x32_f16 v[106:109], v[146:149], v[150:153], v[106:109]
	v_add_u32_e32 v182, 34, v130
	v_bitop3_b32 v183, v182, v129, 6 bitop3:0x6c
	v_lshl_add_u32 v182, v182, 7, 0
	v_mfma_f32_16x16x32_f16 v[94:97], v[142:145], v[154:157], v[94:97]
	ds_read_b128 v[22:25], v175 offset:2048
	v_mfma_f32_16x16x32_f16 v[90:93], v[146:149], v[154:157], v[90:93]
	v_lshl_or_b32 v176, v183, 4, v182
	v_xor_b32_e32 v176, s81, v176
	v_mfma_f32_16x16x32_f16 v[74:77], v[142:145], v[158:161], v[74:77]
	ds_read_b128 v[42:45], v176
	v_mfma_f32_16x16x32_f16 v[58:61], v[146:149], v[158:161], v[58:61]
	v_mfma_f32_16x16x32_f16 v[78:81], v[142:145], v[162:165], v[78:81]
	ds_read_b128 v[38:41], v176 offset:2048
	v_mfma_f32_16x16x32_f16 v[62:65], v[146:149], v[162:165], v[62:65]
	s_mov_b32 m0, s72
	s_addk_i32 s34, 0x4000
	global_load_lds_dwordx4 v[180:181], off
	s_waitcnt lgkmcnt(5)
	v_mfma_f32_16x16x32_f16 v[102:105], v[166:169], v[150:153], v[102:105]
	s_waitcnt lgkmcnt(4)
	v_mfma_f32_16x16x32_f16 v[98:101], v[170:173], v[150:153], v[98:101]
	v_mfma_f32_16x16x32_f16 v[86:89], v[166:169], v[154:157], v[86:89]
	v_mfma_f32_16x16x32_f16 v[82:85], v[170:173], v[154:157], v[82:85]
	v_mfma_f32_16x16x32_f16 v[46:49], v[166:169], v[158:161], v[46:49]
	ds_read_b128 v[54:57], v175 offset:4096
	v_mfma_f32_16x16x32_f16 v[18:21], v[170:173], v[158:161], v[18:21]
	s_add_i32 s61, s61, 1
	s_add_i32 s78, s78, 18
	v_mfma_f32_16x16x32_f16 v[70:73], v[166:169], v[162:165], v[70:73]
	ds_read_b128 v[50:53], v175 offset:6144
	s_cmp_eq_u32 s61, 1
	v_mfma_f32_16x16x32_f16 v[66:69], v[170:173], v[162:165], v[66:69]
	s_cbranch_scc0 .Lc2_loop

.LBB8_14:
	s_or_b64 exec, exec, s[22:23]
	v_lshrrev_b32_e32 v114, 4, v112
	v_bitop3_b32 v7, v114, v0, 6 bitop3:0x78
	v_and_b32_e32 v113, 15, v0
	v_lshlrev_b32_e32 v7, 4, v7
	s_lshr_b32 s23, s28, 8
	v_lshl_or_b32 v7, v113, 7, v7
	v_lshl_or_b32 v6, v8, 6, s37
	s_movk_i32 s22, 0xdc0
	s_and_b32 s30, s3, 3
	v_lshl_or_b32 v7, s23, 13, v7
	s_lshl_b32 s43, s33, 10
	v_and_or_b32 v6, v6, s22, v4
	s_bfe_u32 s22, s2, 0x10003
	s_mul_i32 s2, s30, 0x44
	v_add_u32_e32 v117, 0x18000, v7
	v_or_b32_e32 v7, s43, v5
	v_add_u32_e32 v115, s2, v113
	v_readfirstlane_b32 s2, v7
	s_lshl_b32 s31, s27, 1
	s_mov_b32 m0, s2
	s_lshl_b32 s2, s22, 13
	s_waitcnt lgkmcnt(0)
	s_add_u32 s20, s20, s2
	s_mul_hi_u32 s46, s28, 0x38e38e39
	s_addc_u32 s21, s21, 0
	s_lshr_b32 s47, s46, 9
	s_add_i32 s2, s47, s31
	s_lshl_b32 s35, s3, 11
	s_lshr_b32 s3, s2, 2
	s_add_i32 s3, s3, s31
	s_and_b32 s2, s2, 0x3ffffc
	s_sub_i32 s2, s3, s2
	s_mul_i32 s2, s2, 9
	s_mul_i32 s44, s23, 3
	s_add_i32 s2, s2, s44
	s_ashr_i32 s3, s2, 31
	s_add_i32 s34, s35, 0x18000
	s_lshl_b64 s[2:3], s[2:3], 14
	s_add_u32 s2, s20, s2
	s_addc_u32 s3, s21, s3
	s_mul_i32 s44, s23, -5
	s_add_i32 s44, s44, 6
	s_mul_hi_u32 s45, s44, 0x1c71c71d
	s_add_i32 s45, s45, s31
	s_lshr_b32 s48, s45, 2
	s_add_i32 s48, s48, s31
	s_and_b32 s45, s45, 0x7ffffc
	s_sub_i32 s45, s48, s45
	s_mul_i32 s45, s45, 9
	s_add_i32 s44, s45, s44
	global_load_lds_dwordx4 v[2:3], off
	v_lshlrev_b32_e32 v2, 1, v6
	v_mov_b32_e32 v3, 0
	s_mov_b32 m0, s34
	s_ashr_i32 s45, s44, 31
	v_lshl_add_u64 v[6:7], s[2:3], 0, v[2:3]
	global_load_lds_dwordx4 v2, s[2:3]
	s_mov_b64 s[2:3], 0x400
	s_add_i32 m0, s35, 0x18400
	s_lshl_b64 s[44:45], s[44:45], 14
	v_lshl_add_u64 v[6:7], v[6:7], 0, s[2:3]
	s_add_u32 s44, s20, s44
	global_load_lds_dwordx4 v[6:7], off
	s_addc_u32 s45, s21, s45
	s_add_i32 m0, s35, 0x1c000
	v_lshl_add_u64 v[6:7], s[44:45], 0, v[2:3]
	global_load_lds_dwordx4 v2, s[44:45]
	s_mul_i32 s44, s23, 3
	s_add_i32 s44, s44, 4
	s_mul_hi_u32 s45, s44, 0x1c71c71d
	s_add_i32 s45, s45, s31
	s_lshr_b32 s48, s45, 2
	s_add_i32 s48, s48, s31
	s_and_b32 s45, s45, 0x7ffffc
	s_sub_i32 s45, s48, s45
	s_mul_i32 s45, s45, 9
	s_add_i32 s44, s45, s44
	s_ashr_i32 s45, s44, 31
	s_add_i32 m0, s35, 0x1c400
	s_lshl_b64 s[44:45], s[44:45], 14
	s_add_u32 s44, s20, s44
	v_lshl_add_u64 v[6:7], v[6:7], 0, s[2:3]
	s_addc_u32 s45, s21, s45
	global_load_lds_dwordx4 v[6:7], off
	s_add_i32 m0, s35, 0x20000
	v_lshl_add_u64 v[6:7], s[44:45], 0, v[2:3]
	global_load_lds_dwordx4 v2, s[44:45]
	v_lshl_add_u64 v[6:7], v[6:7], 0, s[2:3]
	s_add_i32 m0, s35, 0x20400
	s_mul_i32 s35, s47, -9
	global_load_lds_dwordx4 v[6:7], off
	s_add_i32 s35, s35, s23
	s_mul_hi_i32 s44, s35, 0x55555556
	s_lshr_b32 s45, s44, 31
	s_add_i32 s44, s44, s45
	s_mul_i32 s44, s44, 31
	s_add_i32 s44, s44, s35
	s_bitcmp1_b32 s46, 9
	s_cselect_b32 s45, 0xc000, 0
	s_or_b32 s39, s39, 64
	v_lshlrev_b32_e32 v52, 1, v4
	v_add_lshl_u32 v4, v32, s39, 6
	s_waitcnt vmcnt(4) lgkmcnt(0)
	s_barrier
	ds_read_b128 v[10:13], v117
	v_add_u32_e32 v14, s44, v115
	v_add3_u32 v32, v4, v50, v33
	v_add_lshl_u32 v4, v42, s39, 6
	v_add_u32_e32 v116, 34, v115
	ds_read_b128 v[6:9], v117 offset:2048
	v_bitop3_b32 v15, v14, v114, 6 bitop3:0x6c
	v_lshl_add_u32 v14, v14, 7, s45
	v_add3_u32 v42, v4, v50, v43
	v_add_lshl_u32 v4, v44, s39, 6
	v_lshl_or_b32 v119, v15, 4, v14
	ds_read_b128 v[18:21], v119
	v_add_u32_e32 v22, s44, v116
	v_add_lshl_u32 v30, v30, s39, 6
	v_add3_u32 v44, v4, v50, v45
	v_add_lshl_u32 v4, v46, s39, 6
	ds_read_b128 v[14:17], v119 offset:2048
	v_bitop3_b32 v23, v22, v114, 6 bitop3:0x6c
	v_lshl_add_u32 v22, v22, 7, s45
	v_add3_u32 v30, v30, v50, v31
	v_add3_u32 v46, v4, v50, v47
	v_add_lshl_u32 v4, v48, s39, 6
	v_lshl_add_u64 v[110:111], s[20:21], 0, v[2:3]
	v_add_u32_e32 v2, s37, v5
	v_lshl_or_b32 v120, v23, 4, v22
	ds_read_b128 v[26:29], v120
	v_ashrrev_i32_e32 v31, 31, v30
	v_add3_u32 v48, v4, v50, v49
	v_add_u32_e32 v121, 0xc000, v2
	v_add_u32_e32 v2, s38, v5
	ds_read_b128 v[22:25], v120 offset:2048
	v_lshlrev_b64 v[30:31], 7, v[30:31]
	v_ashrrev_i32_e32 v33, 31, v32
	v_ashrrev_i32_e32 v43, 31, v42
	v_ashrrev_i32_e32 v45, 31, v44
	v_ashrrev_i32_e32 v47, 31, v46
	v_ashrrev_i32_e32 v49, 31, v48
	v_add_u32_e32 v122, 0xc000, v2
	v_add_u32_e32 v2, s40, v5
	ds_read_b128 v[38:41], v117 offset:4096
	v_lshl_add_u64 v[30:31], s[18:19], 0, v[30:31]
	v_mov_b32_e32 v53, v3
	v_lshlrev_b64 v[32:33], 7, v[32:33]
	v_lshlrev_b64 v[42:43], 7, v[42:43]
	v_lshlrev_b64 v[44:45], 7, v[44:45]
	v_lshlrev_b64 v[46:47], 7, v[46:47]
	v_lshlrev_b64 v[48:49], 7, v[48:49]
	v_add_u32_e32 v123, 0xc000, v2
	v_add_u32_e32 v2, s41, v5
	ds_read_b128 v[34:37], v117 offset:6144
	v_lshl_add_u64 v[30:31], v[30:31], 0, v[52:53]
	v_lshl_add_u64 v[32:33], s[18:19], 0, v[32:33]
	v_lshl_add_u64 v[42:43], s[18:19], 0, v[42:43]
	v_lshl_add_u64 v[44:45], s[18:19], 0, v[44:45]
	v_lshl_add_u64 v[46:47], s[18:19], 0, v[46:47]
	v_lshl_add_u64 v[48:49], s[18:19], 0, v[48:49]
	v_mov_b32_e32 v4, s17
	v_add_u32_e32 v124, 0xc000, v2
	v_add_u32_e32 v2, s42, v5
	v_lshl_add_u64 v[32:33], v[32:33], 0, v[52:53]
	v_lshl_add_u64 v[42:43], v[42:43], 0, v[52:53]
	v_lshl_add_u64 v[44:45], v[44:45], 0, v[52:53]
	v_lshl_add_u64 v[46:47], v[46:47], 0, v[52:53]
	v_lshl_add_u64 v[48:49], v[48:49], 0, v[52:53]
	v_cndmask_b32_e32 v99, v4, v31, vcc
	v_mov_b32_e32 v31, s16
	v_add_u32_e32 v125, 0xc000, v2
	v_add_u32_e32 v2, s43, v5
	s_mov_b32 s29, 6
	v_xor_b32_e32 v118, 64, v117
	s_mov_b32 s36, 1
	s_mov_b32 s33, 0
	s_mov_b32 s35, 0xc000
	v_cndmask_b32_e32 v98, v31, v30, vcc
	v_cndmask_b32_e64 v101, v4, v33, s[12:13]
	v_cndmask_b32_e64 v100, v31, v32, s[12:13]
	v_cndmask_b32_e64 v103, v4, v43, s[4:5]
	v_cndmask_b32_e64 v102, v31, v42, s[4:5]
	v_cndmask_b32_e64 v105, v4, v45, s[6:7]
	v_cndmask_b32_e64 v104, v31, v44, s[6:7]
	v_cndmask_b32_e64 v107, v4, v47, s[8:9]
	v_cndmask_b32_e64 v106, v31, v46, s[8:9]
	v_cndmask_b32_e64 v109, v4, v49, s[10:11]
	v_cndmask_b32_e64 v108, v31, v48, s[10:11]
	s_mov_b64 s[4:5], 0
	v_add_u32_e32 v126, 0xc000, v2
	v_mov_b32_e32 v2, v3
	v_mov_b32_e32 v4, v3
	v_mov_b32_e32 v5, v3
	v_mov_b32_e32 v30, v3
	v_mov_b32_e32 v31, v3
	v_mov_b32_e32 v32, v3
	v_mov_b32_e32 v33, v3
	v_mov_b32_e32 v42, v3
	v_mov_b32_e32 v43, v3
	v_mov_b32_e32 v44, v3
	v_mov_b32_e32 v45, v3
	v_mov_b32_e32 v58, v3
	v_mov_b32_e32 v59, v3
	v_mov_b32_e32 v60, v3
	v_mov_b32_e32 v61, v3
	v_mov_b32_e32 v66, v3
	v_mov_b32_e32 v67, v3
	v_mov_b32_e32 v68, v3
	v_mov_b32_e32 v69, v3
	v_mov_b32_e32 v70, v3
	v_mov_b32_e32 v71, v3
	v_mov_b32_e32 v72, v3
	v_mov_b32_e32 v73, v3
	v_mov_b32_e32 v74, v3
	v_mov_b32_e32 v75, v3
	v_mov_b32_e32 v76, v3
	v_mov_b32_e32 v77, v3
	v_mov_b32_e32 v78, v3
	v_mov_b32_e32 v79, v3
	v_mov_b32_e32 v80, v3
	v_mov_b32_e32 v81, v3
	v_mov_b32_e32 v82, v3
	v_mov_b32_e32 v83, v3
	v_mov_b32_e32 v84, v3
	v_mov_b32_e32 v85, v3
	v_mov_b32_e32 v86, v3
	v_mov_b32_e32 v87, v3
	v_mov_b32_e32 v88, v3
	v_mov_b32_e32 v89, v3
	v_mov_b32_e32 v90, v3
	v_mov_b32_e32 v91, v3
	v_mov_b32_e32 v92, v3
	v_mov_b32_e32 v93, v3
	v_mov_b32_e32 v94, v3
	v_mov_b32_e32 v95, v3
	v_mov_b32_e32 v96, v3
	v_mov_b32_e32 v97, v3
	v_mov_b32_e32 v62, v3
	v_mov_b32_e32 v63, v3
	v_mov_b32_e32 v64, v3
	v_mov_b32_e32 v65, v3
	v_mov_b32_e32 v46, v3
	v_mov_b32_e32 v47, v3
	v_mov_b32_e32 v48, v3
	v_mov_b32_e32 v49, v3
	v_mov_b32_e32 v54, v3
	v_mov_b32_e32 v55, v3
	v_mov_b32_e32 v56, v3
	v_mov_b32_e32 v57, v3
	v_mov_b32_e32 v50, v3
	v_mov_b32_e32 v51, v3
	v_mov_b32_e32 v52, v3
	s_mov_b32 s61, 0
	s_mul_i32 s78, s31, 9
	s_mov_b32 s67, 0
	s_mov_b32 s69, 0
	s_mov_b32 s80, 0xc000
	s_lshl_b32 s81, s23, 6
	s_lshl_b32 s79, s23, 13
	v_subrev_u32_e32 v170, s79, v117
	v_xor_b32_e32 v170, s81, v170
	v_add_u32_e32 v171, 0x2000, v170
	v_mov_b32_e32 v160, v171
	v_mov_b32_e32 v168, v115
	v_bitop3_b32 v169, v168, v114, 6 bitop3:0x6c
	v_lshl_add_u32 v168, v168, 7, 0
	v_lshl_or_b32 v162, v169, 4, v168
	v_xor_b32_e32 v162, s81, v162
	v_add_u32_e32 v168, 34, v115
	v_bitop3_b32 v169, v168, v114, 6 bitop3:0x6c
	v_lshl_add_u32 v168, v168, 7, 0
	v_lshl_or_b32 v163, v169, 4, v168
	v_xor_b32_e32 v163, s81, v163
	ds_read_b128 v[10:13], v170
	ds_read_b128 v[6:9], v170 offset:2048
	ds_read_b128 v[38:41], v170 offset:4096
	ds_read_b128 v[34:37], v170 offset:6144
	ds_read_b128 v[18:21], v162
	ds_read_b128 v[14:17], v162 offset:2048
	ds_read_b128 v[26:29], v163
	ds_read_b128 v[22:25], v163 offset:2048
	s_waitcnt lgkmcnt(0)

.Lc5_bar_0:
	s_barrier
	s_waitcnt lgkmcnt(5)
	v_mfma_f32_16x16x32_f16 v[94:97], v[10:13], v[18:21], v[94:97]
	ds_read_b128 v[128:131], v160
	s_mul_i32 s79, s23, 3
	s_add_i32 s79, s79, 2
	s_add_i32 s79, s79, s78
	s_lshl_b32 s68, s79, 14
	s_waitcnt lgkmcnt(5)
	v_mfma_f32_16x16x32_f16 v[90:93], v[6:9], v[18:21], v[90:93]
	v_add_u32_e32 v168, 68, v115
	v_bitop3_b32 v169, v168, v114, 6 bitop3:0x6c
	v_lshl_add_u32 v168, v168, 7, 0
	v_mfma_f32_16x16x32_f16 v[78:81], v[10:13], v[14:17], v[78:81]
	ds_read_b128 v[132:135], v160 offset:2048
	v_lshl_add_u64 v[164:165], v[110:111], 0, s[68:69]
	s_and_b32 s70, s35, 0xc000
	s_add_i32 s70, s70, s34
	v_mfma_f32_16x16x32_f16 v[74:77], v[6:9], v[14:17], v[74:77]
	v_lshl_or_b32 v162, v169, 4, v168
	v_xor_b32_e32 v162, s81, v162
	s_waitcnt lgkmcnt(5)
	v_mfma_f32_16x16x32_f16 v[58:61], v[10:13], v[26:29], v[58:61]
	ds_read_b128 v[136:139], v162
	v_mfma_f32_16x16x32_f16 v[42:45], v[6:9], v[26:29], v[42:45]
	v_add_u32_e32 v168, 102, v115
	v_bitop3_b32 v169, v168, v114, 6 bitop3:0x6c
	v_lshl_add_u32 v168, v168, 7, 0
	s_waitcnt lgkmcnt(5)
	v_mfma_f32_16x16x32_f16 v[62:65], v[10:13], v[22:25], v[62:65]
	ds_read_b128 v[140:143], v162 offset:2048
	v_mfma_f32_16x16x32_f16 v[46:49], v[6:9], v[22:25], v[46:49]
	v_lshl_or_b32 v163, v169, 4, v168
	v_xor_b32_e32 v163, s81, v163
	s_mov_b32 m0, s70
	s_add_i32 s71, s35, 0xffff8000
	global_load_lds_dwordx4 v[164:165], off
	s_waitcnt lgkmcnt(5)
	v_mfma_f32_16x16x32_f16 v[86:89], v[38:41], v[18:21], v[86:89]
	ds_read_b128 v[144:147], v163
	s_waitcnt lgkmcnt(5)
	v_mfma_f32_16x16x32_f16 v[82:85], v[34:37], v[18:21], v[82:85]
	s_and_b32 s71, s71, 0xc000
	s_add_i32 s72, s70, 0x400
	v_lshl_add_u64 v[166:167], v[164:165], 0, s[2:3]
	v_mfma_f32_16x16x32_f16 v[70:73], v[38:41], v[14:17], v[70:73]
	ds_read_b128 v[148:151], v163 offset:2048
	v_mfma_f32_16x16x32_f16 v[66:69], v[34:37], v[14:17], v[66:69]
	v_add_u32_e32 v161, s71, v170
	v_mfma_f32_16x16x32_f16 v[30:33], v[38:41], v[26:29], v[30:33]
	ds_read_b128 v[152:155], v160 offset:4096
	v_mfma_f32_16x16x32_f16 v[2:5], v[34:37], v[26:29], v[2:5]
	v_mfma_f32_16x16x32_f16 v[54:57], v[38:41], v[22:25], v[54:57]
	ds_read_b128 v[156:159], v160 offset:6144
	v_mfma_f32_16x16x32_f16 v[50:53], v[34:37], v[22:25], v[50:53]
	v_add_u32_e32 v160, s71, v171
	s_waitcnt lgkmcnt(7)
	v_mfma_f32_16x16x32_f16 v[94:97], v[128:131], v[26:29], v[94:97]
	ds_read_b128 v[10:13], v161
	s_waitcnt lgkmcnt(7)
	v_mfma_f32_16x16x32_f16 v[90:93], v[132:135], v[26:29], v[90:93]
	v_add_u32_e32 v168, 1, v115
	v_bitop3_b32 v169, v168, v114, 6 bitop3:0x6c
	v_lshl_add_u32 v168, v168, 7, 0
	v_mfma_f32_16x16x32_f16 v[78:81], v[128:131], v[22:25], v[78:81]
	ds_read_b128 v[6:9], v161 offset:2048
	v_mfma_f32_16x16x32_f16 v[74:77], v[132:135], v[22:25], v[74:77]
	v_lshl_or_b32 v162, v169, 4, v168
	v_xor_b32_e32 v162, s81, v162
	s_waitcnt lgkmcnt(7)
	v_mfma_f32_16x16x32_f16 v[58:61], v[128:131], v[136:139], v[58:61]
	ds_read_b128 v[18:21], v162
	v_mfma_f32_16x16x32_f16 v[42:45], v[132:135], v[136:139], v[42:45]
	s_waitcnt lgkmcnt(7)
	v_mfma_f32_16x16x32_f16 v[62:65], v[128:131], v[140:143], v[62:65]
	ds_read_b128 v[14:17], v162 offset:2048
	v_mfma_f32_16x16x32_f16 v[46:49], v[132:135], v[140:143], v[46:49]
	s_mov_b32 m0, s72
	s_addk_i32 s35, 0x4000
	global_load_lds_dwordx4 v[166:167], off
	s_waitcnt lgkmcnt(5)
	v_mfma_f32_16x16x32_f16 v[86:89], v[152:155], v[26:29], v[86:89]
	s_waitcnt lgkmcnt(4)
	v_mfma_f32_16x16x32_f16 v[82:85], v[156:159], v[26:29], v[82:85]
	v_mfma_f32_16x16x32_f16 v[70:73], v[152:155], v[22:25], v[70:73]
	v_mfma_f32_16x16x32_f16 v[66:69], v[156:159], v[22:25], v[66:69]
	v_mfma_f32_16x16x32_f16 v[30:33], v[152:155], v[136:139], v[30:33]
	ds_read_b128 v[38:41], v161 offset:4096
	v_mfma_f32_16x16x32_f16 v[2:5], v[156:159], v[136:139], v[2:5]
	v_mfma_f32_16x16x32_f16 v[54:57], v[152:155], v[140:143], v[54:57]
	ds_read_b128 v[34:37], v161 offset:6144
	v_mfma_f32_16x16x32_f16 v[50:53], v[156:159], v[140:143], v[50:53]
	v_readfirstlane_b32 s4, v121
	s_mov_b32 m0, s4
	v_readfirstlane_b32 s4, v122
	global_load_lds_dwordx4 v[98:99], off
	s_mov_b32 m0, s4
	v_readfirstlane_b32 s4, v123
	global_load_lds_dwordx4 v[100:101], off
	s_mov_b32 m0, s4
	v_readfirstlane_b32 s4, v124
	global_load_lds_dwordx4 v[102:103], off
	s_mov_b32 m0, s4
	v_readfirstlane_b32 s4, v125
	global_load_lds_dwordx4 v[104:105], off
	s_mov_b32 m0, s4
	v_readfirstlane_b32 s4, v126
	global_load_lds_dwordx4 v[106:107], off
	s_mov_b32 m0, s4
	s_mov_b64 s[4:5], -1
	global_load_lds_dwordx4 v[108:109], off
	s_mov_b32 s67, 2
	s_cmp_eq_u32 s67, 0
	s_cbranch_scc1 .Lc5_w2_1
	s_waitcnt vmcnt(8)
	s_sub_i32 s67, s67, 1
	s_branch .Lc5_bar_1

.Lc5_bar_1:
	s_barrier
	s_waitcnt lgkmcnt(5)
	v_mfma_f32_16x16x32_f16 v[94:97], v[10:13], v[136:139], v[94:97]
	ds_read_b128 v[128:131], v160
	s_mul_i32 s79, s23, 1
	s_add_i32 s79, s79, 8
	s_add_i32 s79, s79, s78
	s_lshl_b32 s68, s79, 14
	s_waitcnt lgkmcnt(5)
	v_mfma_f32_16x16x32_f16 v[90:93], v[6:9], v[136:139], v[90:93]
	v_add_u32_e32 v168, 35, v115
	v_bitop3_b32 v169, v168, v114, 6 bitop3:0x6c
	v_lshl_add_u32 v168, v168, 7, 0
	v_mfma_f32_16x16x32_f16 v[78:81], v[10:13], v[140:143], v[78:81]
	ds_read_b128 v[132:135], v160 offset:2048
	v_lshl_add_u64 v[164:165], v[110:111], 0, s[68:69]
	s_and_b32 s70, s35, 0xc000
	s_add_i32 s70, s70, s34
	v_mfma_f32_16x16x32_f16 v[74:77], v[6:9], v[140:143], v[74:77]
	v_lshl_or_b32 v162, v169, 4, v168
	v_xor_b32_e32 v162, s81, v162
	v_mfma_f32_16x16x32_f16 v[58:61], v[10:13], v[144:147], v[58:61]
	ds_read_b128 v[26:29], v162
	v_mfma_f32_16x16x32_f16 v[42:45], v[6:9], v[144:147], v[42:45]
	v_mfma_f32_16x16x32_f16 v[62:65], v[10:13], v[148:151], v[62:65]
	ds_read_b128 v[22:25], v162 offset:2048
	v_mfma_f32_16x16x32_f16 v[46:49], v[6:9], v[148:151], v[46:49]
	s_mov_b32 m0, s70
	s_add_i32 s71, s35, 0xffff8000
	global_load_lds_dwordx4 v[164:165], off
	s_waitcnt lgkmcnt(5)
	v_mfma_f32_16x16x32_f16 v[86:89], v[38:41], v[136:139], v[86:89]
	s_waitcnt lgkmcnt(4)
	v_mfma_f32_16x16x32_f16 v[82:85], v[34:37], v[136:139], v[82:85]
	s_and_b32 s71, s71, 0xc000
	s_add_i32 s72, s70, 0x400
	v_lshl_add_u64 v[166:167], v[164:165], 0, s[2:3]
	v_mfma_f32_16x16x32_f16 v[70:73], v[38:41], v[140:143], v[70:73]
	v_mfma_f32_16x16x32_f16 v[66:69], v[34:37], v[140:143], v[66:69]
	v_add_u32_e32 v161, s71, v170
	v_mfma_f32_16x16x32_f16 v[30:33], v[38:41], v[144:147], v[30:33]
	ds_read_b128 v[152:155], v160 offset:4096
	v_mfma_f32_16x16x32_f16 v[2:5], v[34:37], v[144:147], v[2:5]
	v_mfma_f32_16x16x32_f16 v[54:57], v[38:41], v[148:151], v[54:57]
	ds_read_b128 v[156:159], v160 offset:6144
	v_mfma_f32_16x16x32_f16 v[50:53], v[34:37], v[148:151], v[50:53]
	v_add_u32_e32 v160, s71, v171
	s_waitcnt lgkmcnt(5)
	v_mfma_f32_16x16x32_f16 v[94:97], v[128:131], v[18:21], v[94:97]
	ds_read_b128 v[10:13], v161
	s_waitcnt lgkmcnt(5)
	v_mfma_f32_16x16x32_f16 v[90:93], v[132:135], v[18:21], v[90:93]
	v_add_u32_e32 v168, 69, v115
	v_bitop3_b32 v169, v168, v114, 6 bitop3:0x6c
	v_lshl_add_u32 v168, v168, 7, 0
	v_mfma_f32_16x16x32_f16 v[78:81], v[128:131], v[14:17], v[78:81]
	ds_read_b128 v[6:9], v161 offset:2048
	v_mfma_f32_16x16x32_f16 v[74:77], v[132:135], v[14:17], v[74:77]
	v_lshl_or_b32 v162, v169, 4, v168
	v_xor_b32_e32 v162, s81, v162
	s_waitcnt lgkmcnt(5)
	v_mfma_f32_16x16x32_f16 v[58:61], v[128:131], v[26:29], v[58:61]
	ds_read_b128 v[136:139], v162
	v_mfma_f32_16x16x32_f16 v[42:45], v[132:135], v[26:29], v[42:45]
	v_add_u32_e32 v168, 103, v115
	v_bitop3_b32 v169, v168, v114, 6 bitop3:0x6c
	v_lshl_add_u32 v168, v168, 7, 0
	s_waitcnt lgkmcnt(5)
	v_mfma_f32_16x16x32_f16 v[62:65], v[128:131], v[22:25], v[62:65]
	ds_read_b128 v[140:143], v162 offset:2048
	v_mfma_f32_16x16x32_f16 v[46:49], v[132:135], v[22:25], v[46:49]
	v_lshl_or_b32 v163, v169, 4, v168
	v_xor_b32_e32 v163, s81, v163
	s_mov_b32 m0, s72
	s_addk_i32 s35, 0x4000
	global_load_lds_dwordx4 v[166:167], off
	s_waitcnt lgkmcnt(5)
	v_mfma_f32_16x16x32_f16 v[86:89], v[152:155], v[18:21], v[86:89]
	ds_read_b128 v[144:147], v163
	s_waitcnt lgkmcnt(5)
	v_mfma_f32_16x16x32_f16 v[82:85], v[156:159], v[18:21], v[82:85]
	v_mfma_f32_16x16x32_f16 v[70:73], v[152:155], v[14:17], v[70:73]
	ds_read_b128 v[148:151], v163 offset:2048
	v_mfma_f32_16x16x32_f16 v[66:69], v[156:159], v[14:17], v[66:69]
	v_mfma_f32_16x16x32_f16 v[30:33], v[152:155], v[26:29], v[30:33]
	ds_read_b128 v[38:41], v161 offset:4096
	v_mfma_f32_16x16x32_f16 v[2:5], v[156:159], v[26:29], v[2:5]
	v_mfma_f32_16x16x32_f16 v[54:57], v[152:155], v[22:25], v[54:57]
	ds_read_b128 v[34:37], v161 offset:6144
	v_mfma_f32_16x16x32_f16 v[50:53], v[156:159], v[22:25], v[50:53]
	s_cmp_eq_u32 s67, 0
	s_cbranch_scc1 .Lc5_w2_2
	s_waitcnt vmcnt(8)
	s_sub_i32 s67, s67, 1
	s_branch .Lc5_bar_2

.Lc5_bar_2:
	s_barrier
	s_waitcnt lgkmcnt(7)
	v_mfma_f32_16x16x32_f16 v[94:97], v[10:13], v[26:29], v[94:97]
	ds_read_b128 v[128:131], v160
	s_mul_i32 s79, s23, 3
	s_add_i32 s79, s79, 12
	s_add_i32 s79, s79, s78
	s_lshl_b32 s68, s79, 14
	s_waitcnt lgkmcnt(7)
	v_mfma_f32_16x16x32_f16 v[90:93], v[6:9], v[26:29], v[90:93]
	v_add_u32_e32 v168, 2, v115
	v_bitop3_b32 v169, v168, v114, 6 bitop3:0x6c
	v_lshl_add_u32 v168, v168, 7, 0
	v_mfma_f32_16x16x32_f16 v[78:81], v[10:13], v[22:25], v[78:81]
	ds_read_b128 v[132:135], v160 offset:2048
	v_lshl_add_u64 v[164:165], v[110:111], 0, s[68:69]
	s_and_b32 s70, s35, 0xc000
	s_add_i32 s70, s70, s34
	v_mfma_f32_16x16x32_f16 v[74:77], v[6:9], v[22:25], v[74:77]
	v_lshl_or_b32 v162, v169, 4, v168
	v_xor_b32_e32 v162, s81, v162
	s_waitcnt lgkmcnt(7)
	v_mfma_f32_16x16x32_f16 v[58:61], v[10:13], v[136:139], v[58:61]
	ds_read_b128 v[18:21], v162
	v_mfma_f32_16x16x32_f16 v[42:45], v[6:9], v[136:139], v[42:45]
	s_waitcnt lgkmcnt(7)
	v_mfma_f32_16x16x32_f16 v[62:65], v[10:13], v[140:143], v[62:65]
	ds_read_b128 v[14:17], v162 offset:2048
	v_mfma_f32_16x16x32_f16 v[46:49], v[6:9], v[140:143], v[46:49]
	s_mov_b32 m0, s70
	s_add_i32 s71, s35, 0xffff8000
	global_load_lds_dwordx4 v[164:165], off
	s_waitcnt lgkmcnt(5)
	v_mfma_f32_16x16x32_f16 v[86:89], v[38:41], v[26:29], v[86:89]
	s_waitcnt lgkmcnt(4)
	v_mfma_f32_16x16x32_f16 v[82:85], v[34:37], v[26:29], v[82:85]
	s_and_b32 s71, s71, 0xc000
	s_add_i32 s72, s70, 0x400
	v_lshl_add_u64 v[166:167], v[164:165], 0, s[2:3]
	v_mfma_f32_16x16x32_f16 v[70:73], v[38:41], v[22:25], v[70:73]
	v_mfma_f32_16x16x32_f16 v[66:69], v[34:37], v[22:25], v[66:69]
	v_add_u32_e32 v161, s71, v170
	v_mfma_f32_16x16x32_f16 v[30:33], v[38:41], v[136:139], v[30:33]
	ds_read_b128 v[152:155], v160 offset:4096
	v_mfma_f32_16x16x32_f16 v[2:5], v[34:37], v[136:139], v[2:5]
	v_mfma_f32_16x16x32_f16 v[54:57], v[38:41], v[140:143], v[54:57]
	ds_read_b128 v[156:159], v160 offset:6144
	v_mfma_f32_16x16x32_f16 v[50:53], v[34:37], v[140:143], v[50:53]
	v_add_u32_e32 v160, s71, v171
	s_waitcnt lgkmcnt(5)
	v_mfma_f32_16x16x32_f16 v[94:97], v[128:131], v[136:139], v[94:97]
	ds_read_b128 v[10:13], v161
	s_waitcnt lgkmcnt(5)
	v_mfma_f32_16x16x32_f16 v[90:93], v[132:135], v[136:139], v[90:93]
	v_add_u32_e32 v168, 36, v115
	v_bitop3_b32 v169, v168, v114, 6 bitop3:0x6c
	v_lshl_add_u32 v168, v168, 7, 0
	v_mfma_f32_16x16x32_f16 v[78:81], v[128:131], v[140:143], v[78:81]
	ds_read_b128 v[6:9], v161 offset:2048
	v_mfma_f32_16x16x32_f16 v[74:77], v[132:135], v[140:143], v[74:77]
	v_lshl_or_b32 v162, v169, 4, v168
	v_xor_b32_e32 v162, s81, v162
	v_mfma_f32_16x16x32_f16 v[58:61], v[128:131], v[144:147], v[58:61]
	ds_read_b128 v[26:29], v162
	v_mfma_f32_16x16x32_f16 v[42:45], v[132:135], v[144:147], v[42:45]
	v_mfma_f32_16x16x32_f16 v[62:65], v[128:131], v[148:151], v[62:65]
	ds_read_b128 v[22:25], v162 offset:2048
	v_mfma_f32_16x16x32_f16 v[46:49], v[132:135], v[148:151], v[46:49]
	s_mov_b32 m0, s72
	s_addk_i32 s35, 0x4000
	global_load_lds_dwordx4 v[166:167], off
	s_waitcnt lgkmcnt(5)
	v_mfma_f32_16x16x32_f16 v[86:89], v[152:155], v[136:139], v[86:89]
	s_waitcnt lgkmcnt(4)
	v_mfma_f32_16x16x32_f16 v[82:85], v[156:159], v[136:139], v[82:85]
	v_mfma_f32_16x16x32_f16 v[70:73], v[152:155], v[140:143], v[70:73]
	v_mfma_f32_16x16x32_f16 v[66:69], v[156:159], v[140:143], v[66:69]
	v_mfma_f32_16x16x32_f16 v[30:33], v[152:155], v[144:147], v[30:33]
	ds_read_b128 v[38:41], v161 offset:4096
	v_mfma_f32_16x16x32_f16 v[2:5], v[156:159], v[144:147], v[2:5]
	v_mfma_f32_16x16x32_f16 v[54:57], v[152:155], v[148:151], v[54:57]
	ds_read_b128 v[34:37], v161 offset:6144
	v_mfma_f32_16x16x32_f16 v[50:53], v[156:159], v[148:151], v[50:53]
	s_cmp_eq_u32 s67, 0
	s_cbranch_scc1 .Lc5_w2_3
	s_waitcnt vmcnt(8)
	s_sub_i32 s67, s67, 1
	s_branch .Lc5_bar_3

.Lc5_bar_3:
	s_barrier
	s_waitcnt lgkmcnt(5)
	v_mfma_f32_16x16x32_f16 v[94:97], v[10:13], v[18:21], v[94:97]
	ds_read_b128 v[128:131], v160
	s_mul_i32 s79, s23, 3
	s_add_i32 s79, s79, 10
	s_add_i32 s79, s79, s78
	s_lshl_b32 s68, s79, 14
	s_waitcnt lgkmcnt(5)
	v_mfma_f32_16x16x32_f16 v[90:93], v[6:9], v[18:21], v[90:93]
	v_add_u32_e32 v168, 70, v115
	v_bitop3_b32 v169, v168, v114, 6 bitop3:0x6c
	v_lshl_add_u32 v168, v168, 7, 0
	v_mfma_f32_16x16x32_f16 v[78:81], v[10:13], v[14:17], v[78:81]
	ds_read_b128 v[132:135], v160 offset:2048
	v_lshl_add_u64 v[164:165], v[110:111], 0, s[68:69]
	s_and_b32 s70, s35, 0xc000
	s_add_i32 s70, s70, s34
	v_mfma_f32_16x16x32_f16 v[74:77], v[6:9], v[14:17], v[74:77]
	v_lshl_or_b32 v162, v169, 4, v168
	v_xor_b32_e32 v162, s81, v162
	s_waitcnt lgkmcnt(5)
	v_mfma_f32_16x16x32_f16 v[58:61], v[10:13], v[26:29], v[58:61]
	ds_read_b128 v[136:139], v162
	v_mfma_f32_16x16x32_f16 v[42:45], v[6:9], v[26:29], v[42:45]
	v_add_u32_e32 v168, 104, v115
	v_bitop3_b32 v169, v168, v114, 6 bitop3:0x6c
	v_lshl_add_u32 v168, v168, 7, 0
	s_waitcnt lgkmcnt(5)
	v_mfma_f32_16x16x32_f16 v[62:65], v[10:13], v[22:25], v[62:65]
	ds_read_b128 v[140:143], v162 offset:2048
	v_mfma_f32_16x16x32_f16 v[46:49], v[6:9], v[22:25], v[46:49]
	v_lshl_or_b32 v163, v169, 4, v168
	v_xor_b32_e32 v163, s81, v163
	s_mov_b32 m0, s70
	s_add_i32 s71, s35, 0xffff8000
	global_load_lds_dwordx4 v[164:165], off
	s_waitcnt lgkmcnt(5)
	v_mfma_f32_16x16x32_f16 v[86:89], v[38:41], v[18:21], v[86:89]
	ds_read_b128 v[144:147], v163
	s_waitcnt lgkmcnt(5)
	v_mfma_f32_16x16x32_f16 v[82:85], v[34:37], v[18:21], v[82:85]
	s_and_b32 s71, s71, 0xc000
	s_add_i32 s72, s70, 0x400
	v_lshl_add_u64 v[166:167], v[164:165], 0, s[2:3]
	v_mfma_f32_16x16x32_f16 v[70:73], v[38:41], v[14:17], v[70:73]
	ds_read_b128 v[148:151], v163 offset:2048
	v_mfma_f32_16x16x32_f16 v[66:69], v[34:37], v[14:17], v[66:69]
	v_add_u32_e32 v161, s71, v170
	v_mfma_f32_16x16x32_f16 v[30:33], v[38:41], v[26:29], v[30:33]
	ds_read_b128 v[152:155], v160 offset:4096
	v_mfma_f32_16x16x32_f16 v[2:5], v[34:37], v[26:29], v[2:5]
	v_mfma_f32_16x16x32_f16 v[54:57], v[38:41], v[22:25], v[54:57]
	ds_read_b128 v[156:159], v160 offset:6144
	v_mfma_f32_16x16x32_f16 v[50:53], v[34:37], v[22:25], v[50:53]
	v_add_u32_e32 v160, s71, v171
	s_waitcnt lgkmcnt(7)
	v_mfma_f32_16x16x32_f16 v[94:97], v[128:131], v[26:29], v[94:97]
	ds_read_b128 v[10:13], v161
	s_waitcnt lgkmcnt(7)
	v_mfma_f32_16x16x32_f16 v[90:93], v[132:135], v[26:29], v[90:93]
	v_mov_b32_e32 v168, v115
	v_bitop3_b32 v169, v168, v114, 6 bitop3:0x6c
	v_lshl_add_u32 v168, v168, 7, s80
	v_mfma_f32_16x16x32_f16 v[78:81], v[128:131], v[22:25], v[78:81]
	ds_read_b128 v[6:9], v161 offset:2048
	v_mfma_f32_16x16x32_f16 v[74:77], v[132:135], v[22:25], v[74:77]
	v_lshl_or_b32 v162, v169, 4, v168
	v_xor_b32_e32 v162, s81, v162
	s_waitcnt lgkmcnt(7)
	v_mfma_f32_16x16x32_f16 v[58:61], v[128:131], v[136:139], v[58:61]
	ds_read_b128 v[18:21], v162
	v_mfma_f32_16x16x32_f16 v[42:45], v[132:135], v[136:139], v[42:45]
	s_waitcnt lgkmcnt(7)
	v_mfma_f32_16x16x32_f16 v[62:65], v[128:131], v[140:143], v[62:65]
	ds_read_b128 v[14:17], v162 offset:2048
	v_mfma_f32_16x16x32_f16 v[46:49], v[132:135], v[140:143], v[46:49]
	s_mov_b32 m0, s72
	s_addk_i32 s35, 0x4000
	global_load_lds_dwordx4 v[166:167], off
	s_waitcnt lgkmcnt(5)
	v_mfma_f32_16x16x32_f16 v[86:89], v[152:155], v[26:29], v[86:89]
	s_waitcnt lgkmcnt(4)
	v_mfma_f32_16x16x32_f16 v[82:85], v[156:159], v[26:29], v[82:85]
	v_mfma_f32_16x16x32_f16 v[70:73], v[152:155], v[22:25], v[70:73]
	v_mfma_f32_16x16x32_f16 v[66:69], v[156:159], v[22:25], v[66:69]
	v_mfma_f32_16x16x32_f16 v[30:33], v[152:155], v[136:139], v[30:33]
	ds_read_b128 v[38:41], v161 offset:4096
	v_mfma_f32_16x16x32_f16 v[2:5], v[156:159], v[136:139], v[2:5]
	v_mfma_f32_16x16x32_f16 v[54:57], v[152:155], v[140:143], v[54:57]
	ds_read_b128 v[34:37], v161 offset:6144
	v_mfma_f32_16x16x32_f16 v[50:53], v[156:159], v[140:143], v[50:53]
	s_cmp_eq_u32 s67, 0
	s_cbranch_scc1 .Lc5_w2_4
	s_waitcnt vmcnt(8)
	s_sub_i32 s67, s67, 1
	s_branch .Lc5_bar_4

.Lc5_bar_4:
	s_barrier
	s_waitcnt lgkmcnt(5)
	v_mfma_f32_16x16x32_f16 v[94:97], v[10:13], v[136:139], v[94:97]
	ds_read_b128 v[128:131], v160
	s_mul_i32 s79, s23, -5
	s_add_i32 s79, s79, 16
	s_add_i32 s79, s79, s78
	s_lshl_b32 s68, s79, 14
	s_waitcnt lgkmcnt(5)
	v_mfma_f32_16x16x32_f16 v[90:93], v[6:9], v[136:139], v[90:93]
	v_add_u32_e32 v168, 34, v115
	v_bitop3_b32 v169, v168, v114, 6 bitop3:0x6c
	v_lshl_add_u32 v168, v168, 7, s80
	v_mfma_f32_16x16x32_f16 v[78:81], v[10:13], v[140:143], v[78:81]
	ds_read_b128 v[132:135], v160 offset:2048
	v_lshl_add_u64 v[164:165], v[110:111], 0, s[68:69]
	s_and_b32 s70, s35, 0xc000
	s_add_i32 s70, s70, s34
	v_mfma_f32_16x16x32_f16 v[74:77], v[6:9], v[140:143], v[74:77]
	v_lshl_or_b32 v162, v169, 4, v168
	v_xor_b32_e32 v162, s81, v162
	v_mfma_f32_16x16x32_f16 v[58:61], v[10:13], v[144:147], v[58:61]
	ds_read_b128 v[26:29], v162
	v_mfma_f32_16x16x32_f16 v[42:45], v[6:9], v[144:147], v[42:45]
	v_mfma_f32_16x16x32_f16 v[62:65], v[10:13], v[148:151], v[62:65]
	ds_read_b128 v[22:25], v162 offset:2048
	v_mfma_f32_16x16x32_f16 v[46:49], v[6:9], v[148:151], v[46:49]
	s_mov_b32 m0, s70
	s_add_i32 s71, s35, 0xffff8000
	global_load_lds_dwordx4 v[164:165], off
	s_waitcnt lgkmcnt(5)
	v_mfma_f32_16x16x32_f16 v[86:89], v[38:41], v[136:139], v[86:89]
	s_waitcnt lgkmcnt(4)
	v_mfma_f32_16x16x32_f16 v[82:85], v[34:37], v[136:139], v[82:85]
	s_and_b32 s71, s71, 0xc000
	s_add_i32 s72, s70, 0x400
	v_lshl_add_u64 v[166:167], v[164:165], 0, s[2:3]
	v_mfma_f32_16x16x32_f16 v[70:73], v[38:41], v[140:143], v[70:73]
	v_mfma_f32_16x16x32_f16 v[66:69], v[34:37], v[140:143], v[66:69]
	v_add_u32_e32 v161, s71, v170
	v_mfma_f32_16x16x32_f16 v[30:33], v[38:41], v[144:147], v[30:33]
	ds_read_b128 v[152:155], v160 offset:4096
	v_mfma_f32_16x16x32_f16 v[2:5], v[34:37], v[144:147], v[2:5]
	v_mfma_f32_16x16x32_f16 v[54:57], v[38:41], v[148:151], v[54:57]
	ds_read_b128 v[156:159], v160 offset:6144
	v_mfma_f32_16x16x32_f16 v[50:53], v[34:37], v[148:151], v[50:53]
	v_add_u32_e32 v160, s71, v171
	s_waitcnt lgkmcnt(5)
	v_mfma_f32_16x16x32_f16 v[94:97], v[128:131], v[18:21], v[94:97]
	ds_read_b128 v[10:13], v161
	s_waitcnt lgkmcnt(5)
	v_mfma_f32_16x16x32_f16 v[90:93], v[132:135], v[18:21], v[90:93]
	v_add_u32_e32 v168, 68, v115
	v_bitop3_b32 v169, v168, v114, 6 bitop3:0x6c
	v_lshl_add_u32 v168, v168, 7, s80
	v_mfma_f32_16x16x32_f16 v[78:81], v[128:131], v[14:17], v[78:81]
	ds_read_b128 v[6:9], v161 offset:2048
	v_mfma_f32_16x16x32_f16 v[74:77], v[132:135], v[14:17], v[74:77]
	v_lshl_or_b32 v162, v169, 4, v168
	v_xor_b32_e32 v162, s81, v162
	s_waitcnt lgkmcnt(5)
	v_mfma_f32_16x16x32_f16 v[58:61], v[128:131], v[26:29], v[58:61]
	ds_read_b128 v[136:139], v162
	v_mfma_f32_16x16x32_f16 v[42:45], v[132:135], v[26:29], v[42:45]
	v_add_u32_e32 v168, 102, v115
	v_bitop3_b32 v169, v168, v114, 6 bitop3:0x6c
	v_lshl_add_u32 v168, v168, 7, s80
	s_waitcnt lgkmcnt(5)
	v_mfma_f32_16x16x32_f16 v[62:65], v[128:131], v[22:25], v[62:65]
	ds_read_b128 v[140:143], v162 offset:2048
	v_mfma_f32_16x16x32_f16 v[46:49], v[132:135], v[22:25], v[46:49]
	v_lshl_or_b32 v163, v169, 4, v168
	v_xor_b32_e32 v163, s81, v163
	s_mov_b32 m0, s72
	s_addk_i32 s35, 0x4000
	global_load_lds_dwordx4 v[166:167], off
	s_waitcnt lgkmcnt(5)
	v_mfma_f32_16x16x32_f16 v[86:89], v[152:155], v[18:21], v[86:89]
	ds_read_b128 v[144:147], v163
	s_waitcnt lgkmcnt(5)
	v_mfma_f32_16x16x32_f16 v[82:85], v[156:159], v[18:21], v[82:85]
	v_mfma_f32_16x16x32_f16 v[70:73], v[152:155], v[14:17], v[70:73]
	ds_read_b128 v[148:151], v163 offset:2048
	v_mfma_f32_16x16x32_f16 v[66:69], v[156:159], v[14:17], v[66:69]
	v_mfma_f32_16x16x32_f16 v[30:33], v[152:155], v[26:29], v[30:33]
	ds_read_b128 v[38:41], v161 offset:4096
	v_mfma_f32_16x16x32_f16 v[2:5], v[156:159], v[26:29], v[2:5]
	v_mfma_f32_16x16x32_f16 v[54:57], v[152:155], v[22:25], v[54:57]
	ds_read_b128 v[34:37], v161 offset:6144
	v_mfma_f32_16x16x32_f16 v[50:53], v[156:159], v[22:25], v[50:53]
	s_cmp_eq_u32 s67, 0
	s_cbranch_scc1 .Lc5_w2_5
	s_waitcnt vmcnt(8)
	s_sub_i32 s67, s67, 1
	s_branch .Lc5_bar_5

.Lc5_bar_5:
	s_barrier
	s_waitcnt lgkmcnt(7)
	v_mfma_f32_16x16x32_f16 v[94:97], v[10:13], v[26:29], v[94:97]
	ds_read_b128 v[128:131], v160
	s_mul_i32 s79, s23, 3
	s_add_i32 s79, s79, 14
	s_add_i32 s79, s79, s78
	s_lshl_b32 s68, s79, 14
	s_waitcnt lgkmcnt(7)
	v_mfma_f32_16x16x32_f16 v[90:93], v[6:9], v[26:29], v[90:93]
	v_add_u32_e32 v168, 1, v115
	v_bitop3_b32 v169, v168, v114, 6 bitop3:0x6c
	v_lshl_add_u32 v168, v168, 7, s80
	v_mfma_f32_16x16x32_f16 v[78:81], v[10:13], v[22:25], v[78:81]
	ds_read_b128 v[132:135], v160 offset:2048
	v_lshl_add_u64 v[164:165], v[110:111], 0, s[68:69]
	s_and_b32 s70, s35, 0xc000
	s_add_i32 s70, s70, s34
	v_mfma_f32_16x16x32_f16 v[74:77], v[6:9], v[22:25], v[74:77]
	v_lshl_or_b32 v162, v169, 4, v168
	v_xor_b32_e32 v162, s81, v162
	s_waitcnt lgkmcnt(7)
	v_mfma_f32_16x16x32_f16 v[58:61], v[10:13], v[136:139], v[58:61]
	ds_read_b128 v[18:21], v162
	v_mfma_f32_16x16x32_f16 v[42:45], v[6:9], v[136:139], v[42:45]
	s_waitcnt lgkmcnt(7)
	v_mfma_f32_16x16x32_f16 v[62:65], v[10:13], v[140:143], v[62:65]
	ds_read_b128 v[14:17], v162 offset:2048
	v_mfma_f32_16x16x32_f16 v[46:49], v[6:9], v[140:143], v[46:49]
	s_mov_b32 m0, s70
	s_add_i32 s71, s35, 0xffff8000
	global_load_lds_dwordx4 v[164:165], off
	s_waitcnt lgkmcnt(5)
	v_mfma_f32_16x16x32_f16 v[86:89], v[38:41], v[26:29], v[86:89]
	s_waitcnt lgkmcnt(4)
	v_mfma_f32_16x16x32_f16 v[82:85], v[34:37], v[26:29], v[82:85]
	s_and_b32 s71, s71, 0xc000
	s_add_i32 s72, s70, 0x400
	v_lshl_add_u64 v[166:167], v[164:165], 0, s[2:3]
	v_mfma_f32_16x16x32_f16 v[70:73], v[38:41], v[22:25], v[70:73]
	v_mfma_f32_16x16x32_f16 v[66:69], v[34:37], v[22:25], v[66:69]
	v_add_u32_e32 v161, s71, v170
	v_mfma_f32_16x16x32_f16 v[30:33], v[38:41], v[136:139], v[30:33]
	ds_read_b128 v[152:155], v160 offset:4096
	v_mfma_f32_16x16x32_f16 v[2:5], v[34:37], v[136:139], v[2:5]
	v_mfma_f32_16x16x32_f16 v[54:57], v[38:41], v[140:143], v[54:57]
	ds_read_b128 v[156:159], v160 offset:6144
	v_mfma_f32_16x16x32_f16 v[50:53], v[34:37], v[140:143], v[50:53]
	v_add_u32_e32 v160, s71, v171
	s_waitcnt lgkmcnt(5)
	v_mfma_f32_16x16x32_f16 v[94:97], v[128:131], v[136:139], v[94:97]
	ds_read_b128 v[10:13], v161
	s_waitcnt lgkmcnt(5)
	v_mfma_f32_16x16x32_f16 v[90:93], v[132:135], v[136:139], v[90:93]
	v_add_u32_e32 v168, 35, v115
	v_bitop3_b32 v169, v168, v114, 6 bitop3:0x6c
	v_lshl_add_u32 v168, v168, 7, s80
	v_mfma_f32_16x16x32_f16 v[78:81], v[128:131], v[140:143], v[78:81]
	ds_read_b128 v[6:9], v161 offset:2048
	v_mfma_f32_16x16x32_f16 v[74:77], v[132:135], v[140:143], v[74:77]
	v_lshl_or_b32 v162, v169, 4, v168
	v_xor_b32_e32 v162, s81, v162
	v_mfma_f32_16x16x32_f16 v[58:61], v[128:131], v[144:147], v[58:61]
	ds_read_b128 v[26:29], v162
	v_mfma_f32_16x16x32_f16 v[42:45], v[132:135], v[144:147], v[42:45]
	v_mfma_f32_16x16x32_f16 v[62:65], v[128:131], v[148:151], v[62:65]
	ds_read_b128 v[22:25], v162 offset:2048
	v_mfma_f32_16x16x32_f16 v[46:49], v[132:135], v[148:151], v[46:49]
	s_mov_b32 m0, s72
	s_addk_i32 s35, 0x4000
	global_load_lds_dwordx4 v[166:167], off
	s_waitcnt lgkmcnt(5)
	v_mfma_f32_16x16x32_f16 v[86:89], v[152:155], v[136:139], v[86:89]
	s_waitcnt lgkmcnt(4)
	v_mfma_f32_16x16x32_f16 v[82:85], v[156:159], v[136:139], v[82:85]
	v_mfma_f32_16x16x32_f16 v[70:73], v[152:155], v[140:143], v[70:73]
	v_mfma_f32_16x16x32_f16 v[66:69], v[156:159], v[140:143], v[66:69]
	v_mfma_f32_16x16x32_f16 v[30:33], v[152:155], v[144:147], v[30:33]
	ds_read_b128 v[38:41], v161 offset:4096
	v_mfma_f32_16x16x32_f16 v[2:5], v[156:159], v[144:147], v[2:5]
	v_mfma_f32_16x16x32_f16 v[54:57], v[152:155], v[148:151], v[54:57]
	ds_read_b128 v[34:37], v161 offset:6144
	v_mfma_f32_16x16x32_f16 v[50:53], v[156:159], v[148:151], v[50:53]
	s_cmp_eq_u32 s67, 0
	s_cbranch_scc1 .Lc5_w2_6
	s_waitcnt vmcnt(8)
	s_sub_i32 s67, s67, 1
	s_branch .Lc5_bar_6

.Lc5_bar_6:
	s_barrier
	s_waitcnt lgkmcnt(5)
	v_mfma_f32_16x16x32_f16 v[94:97], v[10:13], v[18:21], v[94:97]
	ds_read_b128 v[128:131], v160
	s_mul_i32 s79, s23, 0
	s_add_i32 s79, s79, 17
	s_add_i32 s79, s79, s78
	s_lshl_b32 s68, s79, 14
	s_waitcnt lgkmcnt(5)
	v_mfma_f32_16x16x32_f16 v[90:93], v[6:9], v[18:21], v[90:93]
	v_add_u32_e32 v168, 69, v115
	v_bitop3_b32 v169, v168, v114, 6 bitop3:0x6c
	v_lshl_add_u32 v168, v168, 7, s80
	v_mfma_f32_16x16x32_f16 v[78:81], v[10:13], v[14:17], v[78:81]
	ds_read_b128 v[132:135], v160 offset:2048
	v_lshl_add_u64 v[164:165], v[110:111], 0, s[68:69]
	s_and_b32 s70, s35, 0xc000
	s_add_i32 s70, s70, s34
	v_mfma_f32_16x16x32_f16 v[74:77], v[6:9], v[14:17], v[74:77]
	v_lshl_or_b32 v162, v169, 4, v168
	v_xor_b32_e32 v162, s81, v162
	s_waitcnt lgkmcnt(5)
	v_mfma_f32_16x16x32_f16 v[58:61], v[10:13], v[26:29], v[58:61]
	ds_read_b128 v[136:139], v162
	v_mfma_f32_16x16x32_f16 v[42:45], v[6:9], v[26:29], v[42:45]
	v_add_u32_e32 v168, 103, v115
	v_bitop3_b32 v169, v168, v114, 6 bitop3:0x6c
	v_lshl_add_u32 v168, v168, 7, s80
	s_waitcnt lgkmcnt(5)
	v_mfma_f32_16x16x32_f16 v[62:65], v[10:13], v[22:25], v[62:65]
	ds_read_b128 v[140:143], v162 offset:2048
	v_mfma_f32_16x16x32_f16 v[46:49], v[6:9], v[22:25], v[46:49]
	v_lshl_or_b32 v163, v169, 4, v168
	v_xor_b32_e32 v163, s81, v163
	s_mov_b32 m0, s70
	s_add_i32 s71, s35, 0xffff8000
	global_load_lds_dwordx4 v[164:165], off
	s_waitcnt lgkmcnt(5)
	v_mfma_f32_16x16x32_f16 v[86:89], v[38:41], v[18:21], v[86:89]
	ds_read_b128 v[144:147], v163
	s_waitcnt lgkmcnt(5)
	v_mfma_f32_16x16x32_f16 v[82:85], v[34:37], v[18:21], v[82:85]
	s_and_b32 s71, s71, 0xc000
	s_add_i32 s72, s70, 0x400
	v_lshl_add_u64 v[166:167], v[164:165], 0, s[2:3]
	v_mfma_f32_16x16x32_f16 v[70:73], v[38:41], v[14:17], v[70:73]
	ds_read_b128 v[148:151], v163 offset:2048
	v_mfma_f32_16x16x32_f16 v[66:69], v[34:37], v[14:17], v[66:69]
	v_add_u32_e32 v161, s71, v170
	v_mfma_f32_16x16x32_f16 v[30:33], v[38:41], v[26:29], v[30:33]
	ds_read_b128 v[152:155], v160 offset:4096
	v_mfma_f32_16x16x32_f16 v[2:5], v[34:37], v[26:29], v[2:5]
	v_mfma_f32_16x16x32_f16 v[54:57], v[38:41], v[22:25], v[54:57]
	ds_read_b128 v[156:159], v160 offset:6144
	v_mfma_f32_16x16x32_f16 v[50:53], v[34:37], v[22:25], v[50:53]
	v_add_u32_e32 v160, s71, v171
	s_waitcnt lgkmcnt(7)
	v_mfma_f32_16x16x32_f16 v[94:97], v[128:131], v[26:29], v[94:97]
	ds_read_b128 v[10:13], v161
	s_waitcnt lgkmcnt(7)
	v_mfma_f32_16x16x32_f16 v[90:93], v[132:135], v[26:29], v[90:93]
	v_add_u32_e32 v168, 2, v115
	v_bitop3_b32 v169, v168, v114, 6 bitop3:0x6c
	v_lshl_add_u32 v168, v168, 7, s80
	v_mfma_f32_16x16x32_f16 v[78:81], v[128:131], v[22:25], v[78:81]
	ds_read_b128 v[6:9], v161 offset:2048
	v_mfma_f32_16x16x32_f16 v[74:77], v[132:135], v[22:25], v[74:77]
	v_lshl_or_b32 v162, v169, 4, v168
	v_xor_b32_e32 v162, s81, v162
	s_waitcnt lgkmcnt(7)
	v_mfma_f32_16x16x32_f16 v[58:61], v[128:131], v[136:139], v[58:61]
	ds_read_b128 v[18:21], v162
	v_mfma_f32_16x16x32_f16 v[42:45], v[132:135], v[136:139], v[42:45]
	s_waitcnt lgkmcnt(7)
	v_mfma_f32_16x16x32_f16 v[62:65], v[128:131], v[140:143], v[62:65]
	ds_read_b128 v[14:17], v162 offset:2048
	v_mfma_f32_16x16x32_f16 v[46:49], v[132:135], v[140:143], v[46:49]
	s_mov_b32 m0, s72
	s_addk_i32 s35, 0x4000
	global_load_lds_dwordx4 v[166:167], off
	s_waitcnt lgkmcnt(5)
	v_mfma_f32_16x16x32_f16 v[86:89], v[152:155], v[26:29], v[86:89]
	s_waitcnt lgkmcnt(4)
	v_mfma_f32_16x16x32_f16 v[82:85], v[156:159], v[26:29], v[82:85]
	v_mfma_f32_16x16x32_f16 v[70:73], v[152:155], v[22:25], v[70:73]
	v_mfma_f32_16x16x32_f16 v[66:69], v[156:159], v[22:25], v[66:69]
	v_mfma_f32_16x16x32_f16 v[30:33], v[152:155], v[136:139], v[30:33]
	ds_read_b128 v[38:41], v161 offset:4096
	v_mfma_f32_16x16x32_f16 v[2:5], v[156:159], v[136:139], v[2:5]
	v_mfma_f32_16x16x32_f16 v[54:57], v[152:155], v[140:143], v[54:57]
	ds_read_b128 v[34:37], v161 offset:6144
	v_mfma_f32_16x16x32_f16 v[50:53], v[156:159], v[140:143], v[50:53]
	s_cmp_eq_u32 s67, 0
	s_cbranch_scc1 .Lc5_w2_7
	s_waitcnt vmcnt(8)
	s_sub_i32 s67, s67, 1
	s_branch .Lc5_bar_7

.Lc5_bar_7:
	s_barrier
	s_waitcnt lgkmcnt(5)
	v_mfma_f32_16x16x32_f16 v[94:97], v[10:13], v[136:139], v[94:97]
	ds_read_b128 v[128:131], v160
	s_mul_i32 s79, s23, 0
	s_add_i32 s79, s79, 17
	s_add_i32 s79, s79, s78
	s_lshl_b32 s68, s79, 14
	s_waitcnt lgkmcnt(5)
	v_mfma_f32_16x16x32_f16 v[90:93], v[6:9], v[136:139], v[90:93]
	v_add_u32_e32 v168, 36, v115
	v_bitop3_b32 v169, v168, v114, 6 bitop3:0x6c
	v_lshl_add_u32 v168, v168, 7, s80
	v_mfma_f32_16x16x32_f16 v[78:81], v[10:13], v[140:143], v[78:81]
	ds_read_b128 v[132:135], v160 offset:2048
	v_lshl_add_u64 v[164:165], v[110:111], 0, s[68:69]
	s_and_b32 s70, s35, 0xc000
	s_add_i32 s70, s70, s34
	v_mfma_f32_16x16x32_f16 v[74:77], v[6:9], v[140:143], v[74:77]
	v_lshl_or_b32 v162, v169, 4, v168
	v_xor_b32_e32 v162, s81, v162
	v_mfma_f32_16x16x32_f16 v[58:61], v[10:13], v[144:147], v[58:61]
	ds_read_b128 v[26:29], v162
	v_mfma_f32_16x16x32_f16 v[42:45], v[6:9], v[144:147], v[42:45]
	v_mfma_f32_16x16x32_f16 v[62:65], v[10:13], v[148:151], v[62:65]
	ds_read_b128 v[22:25], v162 offset:2048
	v_mfma_f32_16x16x32_f16 v[46:49], v[6:9], v[148:151], v[46:49]
	s_mov_b32 m0, s70
	s_add_i32 s71, s35, 0xffff8000
	global_load_lds_dwordx4 v[164:165], off
	s_waitcnt lgkmcnt(5)
	v_mfma_f32_16x16x32_f16 v[86:89], v[38:41], v[136:139], v[86:89]
	s_waitcnt lgkmcnt(4)
	v_mfma_f32_16x16x32_f16 v[82:85], v[34:37], v[136:139], v[82:85]
	s_and_b32 s71, s71, 0xc000
	s_add_i32 s72, s70, 0x400
	v_lshl_add_u64 v[166:167], v[164:165], 0, s[2:3]
	v_mfma_f32_16x16x32_f16 v[70:73], v[38:41], v[140:143], v[70:73]
	v_mfma_f32_16x16x32_f16 v[66:69], v[34:37], v[140:143], v[66:69]
	v_add_u32_e32 v161, s71, v170
	v_mfma_f32_16x16x32_f16 v[30:33], v[38:41], v[144:147], v[30:33]
	ds_read_b128 v[152:155], v160 offset:4096
	v_mfma_f32_16x16x32_f16 v[2:5], v[34:37], v[144:147], v[2:5]
	v_mfma_f32_16x16x32_f16 v[54:57], v[38:41], v[148:151], v[54:57]
	ds_read_b128 v[156:159], v160 offset:6144
	v_mfma_f32_16x16x32_f16 v[50:53], v[34:37], v[148:151], v[50:53]
	v_add_u32_e32 v160, s71, v171
	s_waitcnt lgkmcnt(5)
	v_mfma_f32_16x16x32_f16 v[94:97], v[128:131], v[18:21], v[94:97]
	ds_read_b128 v[10:13], v161
	s_waitcnt lgkmcnt(5)
	v_mfma_f32_16x16x32_f16 v[90:93], v[132:135], v[18:21], v[90:93]
	v_add_u32_e32 v168, 70, v115
	v_bitop3_b32 v169, v168, v114, 6 bitop3:0x6c
	v_lshl_add_u32 v168, v168, 7, s80
	v_mfma_f32_16x16x32_f16 v[78:81], v[128:131], v[14:17], v[78:81]
	ds_read_b128 v[6:9], v161 offset:2048
	v_mfma_f32_16x16x32_f16 v[74:77], v[132:135], v[14:17], v[74:77]
	v_lshl_or_b32 v162, v169, 4, v168
	v_xor_b32_e32 v162, s81, v162
	s_waitcnt lgkmcnt(5)
	v_mfma_f32_16x16x32_f16 v[58:61], v[128:131], v[26:29], v[58:61]
	ds_read_b128 v[136:139], v162
	v_mfma_f32_16x16x32_f16 v[42:45], v[132:135], v[26:29], v[42:45]
	v_add_u32_e32 v168, 104, v115
	v_bitop3_b32 v169, v168, v114, 6 bitop3:0x6c
	v_lshl_add_u32 v168, v168, 7, s80
	s_waitcnt lgkmcnt(5)
	v_mfma_f32_16x16x32_f16 v[62:65], v[128:131], v[22:25], v[62:65]
	ds_read_b128 v[140:143], v162 offset:2048
	v_mfma_f32_16x16x32_f16 v[46:49], v[132:135], v[22:25], v[46:49]
	v_lshl_or_b32 v163, v169, 4, v168
	v_xor_b32_e32 v163, s81, v163
	s_mov_b32 m0, s72
	s_addk_i32 s35, 0x4000
	global_load_lds_dwordx4 v[166:167], off
	s_waitcnt lgkmcnt(5)
	v_mfma_f32_16x16x32_f16 v[86:89], v[152:155], v[18:21], v[86:89]
	ds_read_b128 v[144:147], v163
	s_waitcnt lgkmcnt(5)
	v_mfma_f32_16x16x32_f16 v[82:85], v[156:159], v[18:21], v[82:85]
	v_mfma_f32_16x16x32_f16 v[70:73], v[152:155], v[14:17], v[70:73]
	ds_read_b128 v[148:151], v163 offset:2048
	v_mfma_f32_16x16x32_f16 v[66:69], v[156:159], v[14:17], v[66:69]
	v_mfma_f32_16x16x32_f16 v[30:33], v[152:155], v[26:29], v[30:33]
	ds_read_b128 v[38:41], v161 offset:4096
	v_mfma_f32_16x16x32_f16 v[2:5], v[156:159], v[26:29], v[2:5]
	v_mfma_f32_16x16x32_f16 v[54:57], v[152:155], v[22:25], v[54:57]
	ds_read_b128 v[34:37], v161 offset:6144
	v_mfma_f32_16x16x32_f16 v[50:53], v[156:159], v[22:25], v[50:53]
	s_cmp_eq_u32 s67, 0
	s_cbranch_scc1 .Lc5_w2_8
	s_waitcnt vmcnt(8)
	s_sub_i32 s67, s67, 1
	s_branch .Lc5_bar_8

.Lc5_bar_8:
	s_barrier
	s_waitcnt lgkmcnt(7)
	v_mfma_f32_16x16x32_f16 v[94:97], v[10:13], v[26:29], v[94:97]
	ds_read_b128 v[128:131], v160
	s_mul_i32 s79, s23, 0
	s_add_i32 s79, s79, 17
	s_add_i32 s79, s79, s78
	s_lshl_b32 s68, s79, 14
	s_waitcnt lgkmcnt(7)
	v_mfma_f32_16x16x32_f16 v[90:93], v[6:9], v[26:29], v[90:93]
	v_mov_b32_e32 v168, v115
	v_bitop3_b32 v169, v168, v114, 6 bitop3:0x6c
	v_lshl_add_u32 v168, v168, 7, 0
	v_mfma_f32_16x16x32_f16 v[78:81], v[10:13], v[22:25], v[78:81]
	ds_read_b128 v[132:135], v160 offset:2048
	v_lshl_add_u64 v[164:165], v[110:111], 0, s[68:69]
	s_and_b32 s70, s35, 0xc000
	s_add_i32 s70, s70, s34
	v_mfma_f32_16x16x32_f16 v[74:77], v[6:9], v[22:25], v[74:77]
	v_lshl_or_b32 v162, v169, 4, v168
	v_xor_b32_e32 v162, s81, v162
	s_waitcnt lgkmcnt(7)
	v_mfma_f32_16x16x32_f16 v[58:61], v[10:13], v[136:139], v[58:61]
	ds_read_b128 v[18:21], v162
	v_mfma_f32_16x16x32_f16 v[42:45], v[6:9], v[136:139], v[42:45]
	s_waitcnt lgkmcnt(7)
	v_mfma_f32_16x16x32_f16 v[62:65], v[10:13], v[140:143], v[62:65]
	ds_read_b128 v[14:17], v162 offset:2048
	v_mfma_f32_16x16x32_f16 v[46:49], v[6:9], v[140:143], v[46:49]
	s_mov_b32 m0, s70
	s_add_i32 s71, s35, 0xffff8000
	global_load_lds_dwordx4 v[164:165], off
	s_waitcnt lgkmcnt(5)
	v_mfma_f32_16x16x32_f16 v[86:89], v[38:41], v[26:29], v[86:89]
	s_waitcnt lgkmcnt(4)
	v_mfma_f32_16x16x32_f16 v[82:85], v[34:37], v[26:29], v[82:85]
	s_and_b32 s71, s71, 0xc000
	s_add_i32 s72, s70, 0x400
	v_lshl_add_u64 v[166:167], v[164:165], 0, s[2:3]
	v_mfma_f32_16x16x32_f16 v[70:73], v[38:41], v[22:25], v[70:73]
	v_mfma_f32_16x16x32_f16 v[66:69], v[34:37], v[22:25], v[66:69]
	v_add_u32_e32 v161, s71, v170
	v_mfma_f32_16x16x32_f16 v[30:33], v[38:41], v[136:139], v[30:33]
	ds_read_b128 v[152:155], v160 offset:4096
	v_mfma_f32_16x16x32_f16 v[2:5], v[34:37], v[136:139], v[2:5]
	v_mfma_f32_16x16x32_f16 v[54:57], v[38:41], v[140:143], v[54:57]
	ds_read_b128 v[156:159], v160 offset:6144
	v_mfma_f32_16x16x32_f16 v[50:53], v[34:37], v[140:143], v[50:53]
	v_add_u32_e32 v160, s71, v171
	s_waitcnt lgkmcnt(5)
	v_mfma_f32_16x16x32_f16 v[94:97], v[128:131], v[136:139], v[94:97]
	ds_read_b128 v[10:13], v161
	s_waitcnt lgkmcnt(5)
	v_mfma_f32_16x16x32_f16 v[90:93], v[132:135], v[136:139], v[90:93]
	v_add_u32_e32 v168, 34, v115
	v_bitop3_b32 v169, v168, v114, 6 bitop3:0x6c
	v_lshl_add_u32 v168, v168, 7, 0
	v_mfma_f32_16x16x32_f16 v[78:81], v[128:131], v[140:143], v[78:81]
	ds_read_b128 v[6:9], v161 offset:2048
	v_mfma_f32_16x16x32_f16 v[74:77], v[132:135], v[140:143], v[74:77]
	v_lshl_or_b32 v162, v169, 4, v168
	v_xor_b32_e32 v162, s81, v162
	v_mfma_f32_16x16x32_f16 v[58:61], v[128:131], v[144:147], v[58:61]
	ds_read_b128 v[26:29], v162
	v_mfma_f32_16x16x32_f16 v[42:45], v[132:135], v[144:147], v[42:45]
	v_mfma_f32_16x16x32_f16 v[62:65], v[128:131], v[148:151], v[62:65]
	ds_read_b128 v[22:25], v162 offset:2048
	v_mfma_f32_16x16x32_f16 v[46:49], v[132:135], v[148:151], v[46:49]
	s_mov_b32 m0, s72
	s_addk_i32 s35, 0x4000
	global_load_lds_dwordx4 v[166:167], off
	s_waitcnt lgkmcnt(5)
	v_mfma_f32_16x16x32_f16 v[86:89], v[152:155], v[136:139], v[86:89]
	s_waitcnt lgkmcnt(4)
	v_mfma_f32_16x16x32_f16 v[82:85], v[156:159], v[136:139], v[82:85]
	v_mfma_f32_16x16x32_f16 v[70:73], v[152:155], v[140:143], v[70:73]
	v_mfma_f32_16x16x32_f16 v[66:69], v[156:159], v[140:143], v[66:69]
	v_mfma_f32_16x16x32_f16 v[30:33], v[152:155], v[144:147], v[30:33]
	ds_read_b128 v[38:41], v161 offset:4096
	v_mfma_f32_16x16x32_f16 v[2:5], v[156:159], v[144:147], v[2:5]
	s_add_i32 s61, s61, 1
	s_add_i32 s78, s78, 18
	v_mfma_f32_16x16x32_f16 v[54:57], v[152:155], v[148:151], v[54:57]
	ds_read_b128 v[34:37], v161 offset:6144
	s_cmp_eq_u32 s61, 1
	v_mfma_f32_16x16x32_f16 v[50:53], v[156:159], v[148:151], v[50:53]
	s_cbranch_scc0 .Lc5_loop
